# P12: next token's selection row loaded mid-token (first one before the loop); loop head no longer drains the previous token's output stores
# baseline (speedup 1.0000x reference)
.LBB0_1203:
	v_readlane_b32 s4, v243, 0
	v_readlane_b32 s6, v243, 2
	s_cmp_lt_i32 s6, 13
	s_cselect_b64 s[0:1], -1, 0
	s_and_b64 s[0:1], s[0:1], s[2:3]
	s_andn2_b64 vcc, exec, s[0:1]
	v_readlane_b32 s5, v243, 1
	v_readlane_b32 s7, v243, 3
	s_cbranch_vccnz .LBB0_1207
	v_readlane_b32 s0, v243, 13
	s_cmpk_gt_i32 s0, 0x1fff
	v_readlane_b32 s1, v243, 14
	s_cbranch_scc1 .LBB0_1207
	s_load_dwordx2 s[2:3], s[96:97], 0xb8
	v_readlane_b32 s42, v243, 13
	v_readlane_b32 s43, v243, 14
	v_and_b32_e32 v0, 63, v0
	v_lshlrev_b32_e32 v126, 4, v0
	s_waitcnt lgkmcnt(0)
	s_add_u32 s8, s2, 0x1ce00000
	s_addc_u32 s9, s3, 0
	s_ashr_i32 s43, s42, 31
	s_lshl_b64 s[0:1], s[42:43], 11
	s_add_u32 s0, s2, s0
	s_addc_u32 s1, s3, s1
	s_add_u32 s10, s0, 0x1ce00000
	s_addc_u32 s11, s1, 0
	s_ashr_i32 s57, s56, 31
	s_lshl_b64 s[12:13], s[56:57], 11
	s_lshl_b64 s[0:1], s[42:43], 5
	s_add_u32 s0, s2, s0
	s_addc_u32 s1, s3, s1
	s_add_u32 s14, s0, 0x300000
	s_addc_u32 s15, s1, 0
	s_add_i32 s0, 0, 0x20140
	v_lshlrev_b32_e32 v127, 6, v0
	s_lshl_b64 s[16:17], s[56:57], 5
	s_lshl_b64 s[18:19], s[42:43], 13
	s_lshl_b64 s[20:21], s[56:57], 13
	v_mov_b32_e32 v5, 0
	s_mov_b32 s23, 0
	s_add_i32 s25, 0, 0x20040
	v_mov_b32_e32 v128, s0
	s_mov_b32 s24, 0x3d800000
	v_mov_b32_e32 v129, 0x358637bd
	s_mov_b32 s28, 0xf800000
	v_mov_b32_e32 v130, 0x260
	global_load_dwordx4 v[62:65], v5, s[14:15]
	global_load_dwordx4 v[70:73], v5, s[14:15] offset:16
	s_waitcnt vmcnt(0)
.LBB0_1206:
	v_mov_b32_e32 v4, v127
	v_mov_b32_e32 v131, v126
	s_ashr_i32 s0, s42, 31
	s_lshr_b32 s0, s0, 20
	s_add_i32 s0, s42, s0
	s_lshr_b32 s0, s0, 12
	ds_read_b32 v10, v128
	s_mulk_i32 s0, 0x3000
	s_ashr_i32 s1, s0, 31
	s_lshl_b64 s[0:1], s[0:1], 2
	s_add_u32 s0, s2, s0
	s_addc_u32 s1, s3, s1
	s_waitcnt lgkmcnt(0)
	v_ashrrev_i32_e32 v11, 31, v10
	v_lshlrev_b64 v[10:11], 19, v[10:11]
	v_lshl_add_u64 v[10:11], s[10:11], 0, v[10:11]
	s_waitcnt vmcnt(8)
	v_readfirstlane_b32 s6, v62
	v_readfirstlane_b32 s7, v63
	v_readfirstlane_b32 s22, v64
	v_readfirstlane_b32 s26, v65
	v_readfirstlane_b32 s27, v70
	v_readfirstlane_b32 s29, v71
	v_readfirstlane_b32 s30, v72
	v_readfirstlane_b32 s31, v73
	s_bfe_u32 s33, s6, 0x100010
	s_lshl_b32 s6, s6, 11
	s_bfe_u32 s34, s7, 0x100010
	s_bfe_u32 s35, s22, 0x100010
	s_lshl_b32 s36, s22, 11
	s_bfe_u32 s37, s26, 0x100010
	s_bfe_u32 s38, s27, 0x100010
	s_bfe_u32 s39, s29, 0x100010
	s_bfe_u32 s40, s30, 0x100010
	s_bfe_u32 s41, s31, 0x100010
	s_lshl_b32 s33, s33, 2
	s_and_b32 s22, s6, 0x7fff800
	s_lshl_b32 s6, s34, 2
	s_lshl_b32 s34, s35, 2
	s_lshl_b32 s35, s37, 2
	s_lshl_b32 s37, s38, 2
	s_lshl_b32 s38, s39, 2
	s_lshl_b32 s39, s40, 2
	s_lshl_b32 s40, s41, 2
	s_add_i32 s33, s25, s33
	s_add_i32 s6, s25, s6
	s_add_i32 s34, s25, s34
	s_add_i32 s35, s25, s35
	s_add_i32 s37, s25, s37
	s_add_i32 s38, s25, s38
	s_add_i32 s39, s25, s39
	s_add_i32 s40, s25, s40
	v_mov_b32_e32 v0, s33
	v_mov_b32_e32 v1, s6
	v_readfirstlane_b32 s4, v10
	v_readfirstlane_b32 s5, v11
	v_mov_b32_e32 v3, s34
	v_mov_b32_e32 v7, s35
	v_mov_b32_e32 v9, s37
	v_mov_b32_e32 v11, s38
	v_mov_b32_e32 v13, s39
	v_mov_b32_e32 v15, s40
	ds_read_b32 v0, v0
	ds_read_b32 v2, v1
	ds_read_b32 v6, v3
	ds_read_b32 v8, v7
	ds_read_b32 v10, v9
	ds_read_b32 v12, v11
	ds_read_b32 v14, v13
	ds_read_b32 v18, v15
	s_waitcnt lgkmcnt(7)
	v_ashrrev_i32_e32 v1, 31, v0
	s_waitcnt lgkmcnt(6)
	v_ashrrev_i32_e32 v3, 31, v2
	v_lshlrev_b64 v[0:1], 19, v[0:1]
	s_lshl_b32 s7, s7, 11
	s_waitcnt lgkmcnt(5)
	v_ashrrev_i32_e32 v7, 31, v6
	v_lshlrev_b64 v[2:3], 19, v[2:3]
	v_lshl_add_u64 v[0:1], s[8:9], 0, v[0:1]
	s_waitcnt lgkmcnt(4)
	v_ashrrev_i32_e32 v9, 31, v8
	v_lshlrev_b64 v[6:7], 19, v[6:7]
	v_lshl_add_u64 v[2:3], s[8:9], 0, v[2:3]
	v_lshl_add_u64 v[136:137], v[0:1], 0, s[22:23]
	s_and_b32 s22, s7, 0x7fff800
	s_lshl_b32 s26, s26, 11
	s_waitcnt lgkmcnt(3)
	v_ashrrev_i32_e32 v11, 31, v10
	v_lshlrev_b64 v[8:9], 19, v[8:9]
	v_lshl_add_u64 v[6:7], s[8:9], 0, v[6:7]
	v_lshl_add_u64 v[140:141], v[2:3], 0, s[22:23]
	s_and_b32 s22, s36, 0x7fff800
	s_lshl_b32 s27, s27, 11
	s_waitcnt lgkmcnt(2)
	v_ashrrev_i32_e32 v13, 31, v12
	v_lshlrev_b64 v[10:11], 19, v[10:11]
	v_lshl_add_u64 v[8:9], s[8:9], 0, v[8:9]
	v_lshl_add_u64 v[148:149], v[6:7], 0, s[22:23]
	s_and_b32 s22, s26, 0x7fff800
	v_lshl_add_u64 v[10:11], s[8:9], 0, v[10:11]
	v_lshl_add_u64 v[64:65], v[8:9], 0, s[22:23]
	s_and_b32 s22, s27, 0x7fff800
	v_lshlrev_b64 v[6:7], 19, v[12:13]
	s_lshl_b32 s6, s29, 11
	v_lshl_add_u64 v[66:67], v[10:11], 0, s[22:23]
	s_and_b32 s22, s6, 0x7fff800
	v_lshl_add_u64 v[6:7], s[8:9], 0, v[6:7]
	s_waitcnt lgkmcnt(1)
	v_ashrrev_i32_e32 v15, 31, v14
	global_load_dwordx4 v[0:3], v131, s[4:5]
	v_lshl_add_u64 v[78:79], v[6:7], 0, s[22:23]
	v_lshlrev_b64 v[6:7], 19, v[14:15]
	global_load_dwordx4 v[14:17], v131, s[4:5] offset:1024
	s_lshl_b32 s4, s30, 11
	s_and_b32 s22, s4, 0x7fff800
	v_lshl_add_u64 v[6:7], s[8:9], 0, v[6:7]
	v_lshl_add_u64 v[6:7], v[6:7], 0, s[22:23]
	s_waitcnt lgkmcnt(0)
	v_ashrrev_i32_e32 v19, 31, v18
	v_readfirstlane_b32 s4, v6
	v_readfirstlane_b32 s5, v7
	v_lshlrev_b64 v[6:7], 19, v[18:19]
	v_lshl_add_u64 v[6:7], s[8:9], 0, v[6:7]
	s_waitcnt vmcnt(1)
	v_cvt_pk_f32_fp8_e32 v[110:111], v0
	s_nop 0
	global_load_dwordx4 v[10:13], v131, s[4:5]
	global_load_dwordx4 v[24:27], v131, s[4:5] offset:1024
	s_lshl_b32 s4, s31, 11
	s_and_b32 s22, s4, 0x7fff800
	v_lshl_add_u64 v[6:7], v[6:7], 0, s[22:23]
	s_add_u32 s0, s0, 0x10a000
	v_readfirstlane_b32 s4, v6
	v_readfirstlane_b32 s5, v7
	s_nop 4
	global_load_dwordx4 v[38:41], v131, s[4:5]
	global_load_dwordx4 v[50:53], v131, s[4:5] offset:1024
	v_readfirstlane_b32 s26, v64
	v_readfirstlane_b32 s27, v65
	s_nop 4
	global_load_dwordx4 v[244:247], v131, s[26:27]
	global_load_dwordx4 v[70:73], v131, s[26:27] offset:1024
	v_readfirstlane_b32 s26, v66
	v_readfirstlane_b32 s27, v67
	s_nop 4
	global_load_dwordx4 v[82:85], v131, s[26:27]
	global_load_dwordx4 v[86:89], v131, s[26:27] offset:1024
	v_readfirstlane_b32 s26, v78
	v_readfirstlane_b32 s27, v79
	s_nop 4
	global_load_dwordx4 v[102:105], v131, s[26:27]
	global_load_dwordx4 v[132:135], v131, s[26:27] offset:1024
	v_readfirstlane_b32 s26, v136
	v_readfirstlane_b32 s27, v137
	s_nop 4
	global_load_dwordx4 v[248:251], v131, s[26:27]
	global_load_dwordx4 v[136:139], v131, s[26:27] offset:1024
	v_readfirstlane_b32 s26, v140
	v_readfirstlane_b32 s27, v141
	s_nop 4
	global_load_dwordx4 v[140:143], v131, s[26:27]
	global_load_dwordx4 v[144:147], v131, s[26:27] offset:1024
	v_readfirstlane_b32 s26, v148
	v_readfirstlane_b32 s27, v149
	s_nop 4
	global_load_dwordx4 v[148:151], v131, s[26:27]
	global_load_dwordx4 v[252:255], v131, s[26:27] offset:1024
	s_load_dwordx4 s[4:7], s[96:97], 0xa8
	v_cvt_pk_f32_fp8_sdwa v[116:117], v0 src0_sel:WORD_1
	v_cvt_pk_f32_fp8_e32 v[112:113], v1
	v_cvt_pk_f32_fp8_sdwa v[118:119], v1 src0_sel:WORD_1
	v_cvt_pk_f32_fp8_e32 v[54:55], v2
	v_cvt_pk_f32_fp8_sdwa v[60:61], v2 src0_sel:WORD_1
	v_cvt_pk_f32_fp8_e32 v[42:43], v3
	v_cvt_pk_f32_fp8_sdwa v[44:45], v3 src0_sel:WORD_1
	s_waitcnt vmcnt(16)
	v_cvt_pk_f32_fp8_e32 v[30:31], v14
	v_cvt_pk_f32_fp8_sdwa v[32:33], v14 src0_sel:WORD_1
	v_cvt_pk_f32_fp8_e32 v[18:19], v15
	v_cvt_pk_f32_fp8_sdwa v[22:23], v15 src0_sel:WORD_1
	v_cvt_pk_f32_fp8_e32 v[2:3], v16
	v_cvt_pk_f32_fp8_sdwa v[8:9], v16 src0_sel:WORD_1
	v_cvt_pk_f32_fp8_e32 v[0:1], v17
	v_cvt_pk_f32_fp8_sdwa v[16:17], v17 src0_sel:WORD_1
	s_addc_u32 s1, s1, 0
	s_waitcnt vmcnt(15)
	v_cvt_pk_f32_fp8_e32 v[152:153], v10
	v_cvt_pk_f32_fp8_sdwa v[154:155], v10 src0_sel:WORD_1
	v_cvt_pk_f32_fp8_e32 v[156:157], v11
	v_cvt_pk_f32_fp8_sdwa v[158:159], v11 src0_sel:WORD_1
	v_cvt_pk_f32_fp8_e32 v[160:161], v12
	v_cvt_pk_f32_fp8_sdwa v[162:163], v12 src0_sel:WORD_1
	v_cvt_pk_f32_fp8_e32 v[62:63], v13
	v_cvt_pk_f32_fp8_sdwa v[68:69], v13 src0_sel:WORD_1
	s_waitcnt vmcnt(14)
	v_cvt_pk_f32_fp8_e32 v[46:47], v24
	v_cvt_pk_f32_fp8_sdwa v[48:49], v24 src0_sel:WORD_1
	v_cvt_pk_f32_fp8_e32 v[34:35], v25
	v_cvt_pk_f32_fp8_sdwa v[36:37], v25 src0_sel:WORD_1
	v_cvt_pk_f32_fp8_e32 v[20:21], v26
	v_cvt_pk_f32_fp8_sdwa v[24:25], v26 src0_sel:WORD_1
	v_cvt_pk_f32_fp8_e32 v[6:7], v27
	v_cvt_pk_f32_fp8_sdwa v[10:11], v27 src0_sel:WORD_1
	s_waitcnt vmcnt(13)
	v_cvt_pk_f32_fp8_e32 v[164:165], v38
	v_cvt_pk_f32_fp8_sdwa v[166:167], v38 src0_sel:WORD_1
	v_cvt_pk_f32_fp8_e32 v[168:169], v39
	v_cvt_pk_f32_fp8_sdwa v[170:171], v39 src0_sel:WORD_1
	v_cvt_pk_f32_fp8_e32 v[90:91], v40
	v_cvt_pk_f32_fp8_sdwa v[92:93], v40 src0_sel:WORD_1
	v_cvt_pk_f32_fp8_e32 v[74:75], v41
	v_cvt_pk_f32_fp8_sdwa v[76:77], v41 src0_sel:WORD_1
	s_waitcnt vmcnt(12)
	v_cvt_pk_f32_fp8_e32 v[56:57], v50
	v_cvt_pk_f32_fp8_sdwa v[58:59], v50 src0_sel:WORD_1
	v_cvt_pk_f32_fp8_e32 v[38:39], v51
	v_cvt_pk_f32_fp8_sdwa v[40:41], v51 src0_sel:WORD_1
	v_cvt_pk_f32_fp8_e32 v[26:27], v52
	v_cvt_pk_f32_fp8_sdwa v[28:29], v52 src0_sel:WORD_1
	v_cvt_pk_f32_fp8_e32 v[12:13], v53
	v_cvt_pk_f32_fp8_sdwa v[14:15], v53 src0_sel:WORD_1
	s_waitcnt vmcnt(11)
	v_cvt_pk_f32_fp8_e32 v[172:173], v244
	v_cvt_pk_f32_fp8_sdwa v[174:175], v244 src0_sel:WORD_1
	v_cvt_pk_f32_fp8_e32 v[176:177], v245
	v_cvt_pk_f32_fp8_sdwa v[178:179], v245 src0_sel:WORD_1
	v_cvt_pk_f32_fp8_e32 v[180:181], v246
	v_cvt_pk_f32_fp8_sdwa v[182:183], v246 src0_sel:WORD_1
	v_cvt_pk_f32_fp8_e32 v[106:107], v247
	v_cvt_pk_f32_fp8_sdwa v[108:109], v247 src0_sel:WORD_1
	s_waitcnt vmcnt(10)
	v_cvt_pk_f32_fp8_e32 v[94:95], v70
	v_cvt_pk_f32_fp8_sdwa v[96:97], v70 src0_sel:WORD_1
	v_cvt_pk_f32_fp8_e32 v[78:79], v71
	v_cvt_pk_f32_fp8_sdwa v[80:81], v71 src0_sel:WORD_1
	v_cvt_pk_f32_fp8_e32 v[64:65], v72
	v_cvt_pk_f32_fp8_sdwa v[66:67], v72 src0_sel:WORD_1
	v_cvt_pk_f32_fp8_e32 v[50:51], v73
	v_cvt_pk_f32_fp8_sdwa v[52:53], v73 src0_sel:WORD_1
	s_waitcnt vmcnt(9)
	v_cvt_pk_f32_fp8_e32 v[184:185], v82
	v_cvt_pk_f32_fp8_sdwa v[186:187], v82 src0_sel:WORD_1
	v_cvt_pk_f32_fp8_e32 v[188:189], v83
	v_cvt_pk_f32_fp8_sdwa v[190:191], v83 src0_sel:WORD_1
	v_cvt_pk_f32_fp8_e32 v[192:193], v84
	v_cvt_pk_f32_fp8_sdwa v[194:195], v84 src0_sel:WORD_1
	v_cvt_pk_f32_fp8_e32 v[196:197], v85
	v_cvt_pk_f32_fp8_sdwa v[198:199], v85 src0_sel:WORD_1
	s_waitcnt vmcnt(8)
	v_cvt_pk_f32_fp8_e32 v[114:115], v86
	v_cvt_pk_f32_fp8_sdwa v[120:121], v86 src0_sel:WORD_1
	v_cvt_pk_f32_fp8_e32 v[98:99], v87
	v_cvt_pk_f32_fp8_sdwa v[100:101], v87 src0_sel:WORD_1
	v_cvt_pk_f32_fp8_e32 v[82:83], v88
	v_cvt_pk_f32_fp8_sdwa v[84:85], v88 src0_sel:WORD_1
	v_cvt_pk_f32_fp8_e32 v[70:71], v89
	v_cvt_pk_f32_fp8_sdwa v[72:73], v89 src0_sel:WORD_1
	s_waitcnt vmcnt(7)
	v_cvt_pk_f32_fp8_e32 v[200:201], v102
	v_cvt_pk_f32_fp8_sdwa v[202:203], v102 src0_sel:WORD_1
	v_cvt_pk_f32_fp8_e32 v[204:205], v103
	v_cvt_pk_f32_fp8_sdwa v[206:207], v103 src0_sel:WORD_1
	v_cvt_pk_f32_fp8_e32 v[208:209], v104
	v_cvt_pk_f32_fp8_sdwa v[210:211], v104 src0_sel:WORD_1
	v_cvt_pk_f32_fp8_e32 v[212:213], v105
	v_cvt_pk_f32_fp8_sdwa v[214:215], v105 src0_sel:WORD_1
	s_waitcnt vmcnt(6)
	v_cvt_pk_f32_fp8_e32 v[216:217], v132
	v_cvt_pk_f32_fp8_sdwa v[218:219], v132 src0_sel:WORD_1
	v_cvt_pk_f32_fp8_e32 v[122:123], v133
	v_cvt_pk_f32_fp8_sdwa v[124:125], v133 src0_sel:WORD_1
	v_cvt_pk_f32_fp8_e32 v[102:103], v134
	v_cvt_pk_f32_fp8_sdwa v[104:105], v134 src0_sel:WORD_1
	v_cvt_pk_f32_fp8_e32 v[86:87], v135
	v_cvt_pk_f32_fp8_sdwa v[88:89], v135 src0_sel:WORD_1
	v_pk_add_f32 v[220:221], v[154:155], 0 op_sel_hi:[1,0]
	v_pk_add_f32 v[222:223], v[152:153], 0 op_sel_hi:[1,0]
	v_pk_add_f32 v[158:159], v[158:159], 0 op_sel_hi:[1,0]
	v_pk_add_f32 v[164:165], v[164:165], v[222:223]
	v_pk_add_f32 v[158:159], v[170:171], v[158:159]
	v_pk_add_f32 v[110:111], v[110:111], v[164:165]
	v_pk_add_f32 v[24:25], v[24:25], 0 op_sel_hi:[1,0]
	v_pk_add_f32 v[20:21], v[20:21], 0 op_sel_hi:[1,0]
	v_pk_add_f32 v[118:119], v[118:119], v[158:159]
	v_pk_add_f32 v[110:111], v[172:173], v[110:111]
	v_pk_add_f32 v[20:21], v[26:27], v[20:21]
	v_pk_add_f32 v[24:25], v[28:29], v[24:25]
	v_pk_add_f32 v[156:157], v[156:157], 0 op_sel_hi:[1,0]
	v_pk_add_f32 v[118:119], v[178:179], v[118:119]
	v_pk_add_f32 v[110:111], v[184:185], v[110:111]
	v_pk_add_f32 v[36:37], v[36:37], 0 op_sel_hi:[1,0]
	v_pk_add_f32 v[34:35], v[34:35], 0 op_sel_hi:[1,0]
	v_pk_add_f32 v[8:9], v[8:9], v[24:25]
	v_pk_add_f32 v[2:3], v[2:3], v[20:21]
	v_pk_add_f32 v[166:167], v[166:167], v[220:221]
	v_pk_add_f32 v[156:157], v[168:169], v[156:157]
	v_pk_add_f32 v[34:35], v[38:39], v[34:35]
	v_pk_add_f32 v[36:37], v[40:41], v[36:37]
	v_pk_add_f32 v[2:3], v[64:65], v[2:3]
	v_pk_add_f32 v[8:9], v[66:67], v[8:9]
	v_pk_add_f32 v[162:163], v[162:163], 0 op_sel_hi:[1,0]
	v_pk_add_f32 v[160:161], v[160:161], 0 op_sel_hi:[1,0]
	v_pk_add_f32 v[116:117], v[116:117], v[166:167]
	v_pk_add_f32 v[112:113], v[112:113], v[156:157]
	v_pk_add_f32 v[68:69], v[68:69], 0 op_sel_hi:[1,0]
	v_pk_add_f32 v[62:63], v[62:63], 0 op_sel_hi:[1,0]
	v_pk_add_f32 v[48:49], v[48:49], 0 op_sel_hi:[1,0]
	v_pk_add_f32 v[46:47], v[46:47], 0 op_sel_hi:[1,0]
	v_pk_add_f32 v[22:23], v[22:23], v[36:37]
	v_pk_add_f32 v[18:19], v[18:19], v[34:35]
	v_pk_add_f32 v[8:9], v[84:85], v[8:9]
	v_pk_add_f32 v[2:3], v[82:83], v[2:3]
	v_pk_add_f32 v[10:11], v[10:11], 0 op_sel_hi:[1,0]
	v_pk_add_f32 v[6:7], v[6:7], 0 op_sel_hi:[1,0]
	v_pk_add_f32 v[116:117], v[174:175], v[116:117]
	v_pk_add_f32 v[112:113], v[176:177], v[112:113]
	v_pk_add_f32 v[90:91], v[90:91], v[160:161]
	v_pk_add_f32 v[92:93], v[92:93], v[162:163]
	v_pk_add_f32 v[62:63], v[74:75], v[62:63]
	v_pk_add_f32 v[68:69], v[76:77], v[68:69]
	v_pk_add_f32 v[46:47], v[56:57], v[46:47]
	v_pk_add_f32 v[48:49], v[58:59], v[48:49]
	v_pk_add_f32 v[2:3], v[102:103], v[2:3]
	v_pk_add_f32 v[8:9], v[104:105], v[8:9]
	v_pk_add_f32 v[6:7], v[12:13], v[6:7]
	v_pk_add_f32 v[10:11], v[14:15], v[10:11]
	v_pk_add_f32 v[116:117], v[186:187], v[116:117]
	v_pk_add_f32 v[118:119], v[190:191], v[118:119]
	v_pk_add_f32 v[112:113], v[188:189], v[112:113]
	v_pk_add_f32 v[60:61], v[60:61], v[92:93]
	v_pk_add_f32 v[54:55], v[54:55], v[90:91]
	v_pk_add_f32 v[44:45], v[44:45], v[68:69]
	v_pk_add_f32 v[42:43], v[42:43], v[62:63]
	v_pk_add_f32 v[32:33], v[32:33], v[48:49]
	v_pk_add_f32 v[30:31], v[30:31], v[46:47]
	v_pk_add_f32 v[10:11], v[16:17], v[10:11]
	v_pk_add_f32 v[0:1], v[0:1], v[6:7]
	v_pk_add_f32 v[110:111], v[200:201], v[110:111]
	v_pk_add_f32 v[116:117], v[202:203], v[116:117]
	v_pk_add_f32 v[112:113], v[204:205], v[112:113]
	v_pk_add_f32 v[118:119], v[206:207], v[118:119]
	v_pk_add_f32 v[54:55], v[180:181], v[54:55]
	v_pk_add_f32 v[60:61], v[182:183], v[60:61]
	v_pk_add_f32 v[42:43], v[106:107], v[42:43]
	v_pk_add_f32 v[44:45], v[108:109], v[44:45]
	v_pk_add_f32 v[30:31], v[94:95], v[30:31]
	s_waitcnt vmcnt(5)
	v_cvt_pk_f32_fp8_e32 v[156:157], v248
	s_waitcnt vmcnt(4)
	v_cvt_pk_f32_fp8_e32 v[178:179], v138
	v_cvt_pk_f32_fp8_sdwa v[184:185], v138 src0_sel:WORD_1
	v_cvt_pk_f32_fp8_sdwa v[158:159], v248 src0_sel:WORD_1
	s_waitcnt vmcnt(2)
	v_cvt_pk_f32_fp8_e32 v[226:227], v146
	v_cvt_pk_f32_fp8_sdwa v[228:229], v146 src0_sel:WORD_1
	v_cvt_pk_f32_fp8_e32 v[164:165], v249
	v_cvt_pk_f32_fp8_sdwa v[132:133], v249 src0_sel:WORD_1
	v_cvt_pk_f32_fp8_e32 v[166:167], v250
	v_cvt_pk_f32_fp8_sdwa v[168:169], v250 src0_sel:WORD_1
	v_cvt_pk_f32_fp8_e32 v[170:171], v251
	v_cvt_pk_f32_fp8_sdwa v[134:135], v251 src0_sel:WORD_1
	v_cvt_pk_f32_fp8_e32 v[172:173], v136
	s_waitcnt vmcnt(0)
	v_cvt_pk_f32_fp8_e32 v[34:35], v254
	v_cvt_pk_f32_fp8_sdwa v[36:37], v254 src0_sel:WORD_1
	v_cvt_pk_f32_fp8_sdwa v[174:175], v136 src0_sel:WORD_1
	v_cvt_pk_f32_fp8_e32 v[176:177], v137
	v_cvt_pk_f32_fp8_sdwa v[136:137], v137 src0_sel:WORD_1
	v_cvt_pk_f32_fp8_e32 v[186:187], v139
	v_cvt_pk_f32_fp8_sdwa v[138:139], v139 src0_sel:WORD_1
	v_pk_add_f32 v[8:9], v[184:185], v[8:9]
	v_pk_add_f32 v[2:3], v[178:179], v[2:3]
	v_cvt_pk_f32_fp8_e32 v[188:189], v140
	v_cvt_pk_f32_fp8_sdwa v[190:191], v140 src0_sel:WORD_1
	v_cvt_pk_f32_fp8_e32 v[200:201], v141
	v_cvt_pk_f32_fp8_sdwa v[140:141], v141 src0_sel:WORD_1
	v_cvt_pk_f32_fp8_e32 v[202:203], v142
	v_cvt_pk_f32_fp8_sdwa v[204:205], v142 src0_sel:WORD_1
	v_cvt_pk_f32_fp8_e32 v[206:207], v143
	v_cvt_pk_f32_fp8_sdwa v[142:143], v143 src0_sel:WORD_1
	v_cvt_pk_f32_fp8_e32 v[220:221], v144
	v_cvt_pk_f32_fp8_sdwa v[222:223], v144 src0_sel:WORD_1
	v_cvt_pk_f32_fp8_e32 v[224:225], v145
	v_cvt_pk_f32_fp8_sdwa v[144:145], v145 src0_sel:WORD_1
	v_cvt_pk_f32_fp8_e32 v[230:231], v147
	v_cvt_pk_f32_fp8_sdwa v[146:147], v147 src0_sel:WORD_1
	v_pk_add_f32 v[32:33], v[96:97], v[32:33]
	v_pk_add_f32 v[18:19], v[78:79], v[18:19]
	v_pk_add_f32 v[22:23], v[80:81], v[22:23]
	v_pk_add_f32 v[2:3], v[226:227], v[2:3]
	v_pk_add_f32 v[8:9], v[228:229], v[8:9]
	v_pk_add_f32 v[0:1], v[50:51], v[0:1]
	v_pk_add_f32 v[6:7], v[52:53], v[10:11]
	v_cvt_pk_f32_fp8_e32 v[232:233], v148
	v_cvt_pk_f32_fp8_sdwa v[234:235], v148 src0_sel:WORD_1
	v_cvt_pk_f32_fp8_e32 v[236:237], v149
	v_cvt_pk_f32_fp8_sdwa v[148:149], v149 src0_sel:WORD_1
	v_cvt_pk_f32_fp8_e32 v[238:239], v150
	v_cvt_pk_f32_fp8_sdwa v[240:241], v150 src0_sel:WORD_1
	v_pk_add_f32 v[60:61], v[194:195], v[60:61]
	v_pk_add_f32 v[54:55], v[192:193], v[54:55]
	v_cvt_pk_f32_fp8_e32 v[90:91], v151
	v_cvt_pk_f32_fp8_sdwa v[92:93], v151 src0_sel:WORD_1
	v_pk_add_f32 v[44:45], v[198:199], v[44:45]
	v_pk_add_f32 v[42:43], v[196:197], v[42:43]
	v_cvt_pk_f32_fp8_e32 v[62:63], v252
	v_cvt_pk_f32_fp8_sdwa v[68:69], v252 src0_sel:WORD_1
	v_pk_add_f32 v[32:33], v[120:121], v[32:33]
	v_pk_add_f32 v[30:31], v[114:115], v[30:31]
	v_cvt_pk_f32_fp8_e32 v[46:47], v253
	v_cvt_pk_f32_fp8_sdwa v[48:49], v253 src0_sel:WORD_1
	v_pk_add_f32 v[22:23], v[100:101], v[22:23]
	v_pk_add_f32 v[18:19], v[98:99], v[18:19]
	v_pk_add_f32 v[20:21], v[36:37], v[8:9]
	v_pk_add_f32 v[24:25], v[34:35], v[2:3]
	v_cvt_pk_f32_fp8_e32 v[2:3], v255
	v_cvt_pk_f32_fp8_sdwa v[8:9], v255 src0_sel:WORD_1
	v_pk_add_f32 v[6:7], v[72:73], v[6:7]
	v_pk_add_f32 v[0:1], v[70:71], v[0:1]
	v_pk_add_f32 v[54:55], v[208:209], v[54:55]
	v_pk_add_f32 v[60:61], v[210:211], v[60:61]
	v_pk_add_f32 v[42:43], v[212:213], v[42:43]
	v_pk_add_f32 v[44:45], v[214:215], v[44:45]
	v_pk_add_f32 v[30:31], v[216:217], v[30:31]
	v_pk_add_f32 v[32:33], v[218:219], v[32:33]
	v_pk_add_f32 v[18:19], v[122:123], v[18:19]
	v_pk_add_f32 v[22:23], v[124:125], v[22:23]
	v_pk_add_f32 v[0:1], v[86:87], v[0:1]
	v_pk_add_f32 v[6:7], v[88:89], v[6:7]
	v_pk_add_f32 v[116:117], v[158:159], v[116:117]
	v_pk_add_f32 v[110:111], v[156:157], v[110:111]
	v_pk_add_f32 v[118:119], v[132:133], v[118:119]
	v_pk_add_f32 v[112:113], v[164:165], v[112:113]
	v_pk_add_f32 v[60:61], v[168:169], v[60:61]
	v_pk_add_f32 v[54:55], v[166:167], v[54:55]
	v_pk_add_f32 v[44:45], v[134:135], v[44:45]
	v_pk_add_f32 v[42:43], v[170:171], v[42:43]
	v_pk_add_f32 v[32:33], v[174:175], v[32:33]
	v_pk_add_f32 v[30:31], v[172:173], v[30:31]
	v_pk_add_f32 v[22:23], v[136:137], v[22:23]
	v_pk_add_f32 v[18:19], v[176:177], v[18:19]
	v_pk_add_f32 v[6:7], v[138:139], v[6:7]
	v_pk_add_f32 v[0:1], v[186:187], v[0:1]
	v_pk_add_f32 v[110:111], v[188:189], v[110:111]
	v_pk_add_f32 v[116:117], v[190:191], v[116:117]
	v_pk_add_f32 v[112:113], v[200:201], v[112:113]
	v_pk_add_f32 v[118:119], v[140:141], v[118:119]
	v_pk_add_f32 v[54:55], v[202:203], v[54:55]
	v_pk_add_f32 v[60:61], v[204:205], v[60:61]
	v_pk_add_f32 v[42:43], v[206:207], v[42:43]
	v_pk_add_f32 v[44:45], v[142:143], v[44:45]
	v_pk_add_f32 v[30:31], v[220:221], v[30:31]
	v_pk_add_f32 v[32:33], v[222:223], v[32:33]
	v_pk_add_f32 v[18:19], v[224:225], v[18:19]
	v_pk_add_f32 v[22:23], v[144:145], v[22:23]
	v_pk_add_f32 v[0:1], v[230:231], v[0:1]
	v_pk_add_f32 v[6:7], v[146:147], v[6:7]
	v_pk_add_f32 v[116:117], v[234:235], v[116:117]
	v_pk_add_f32 v[110:111], v[232:233], v[110:111]
	v_pk_add_f32 v[118:119], v[148:149], v[118:119]
	v_pk_add_f32 v[112:113], v[236:237], v[112:113]
	v_pk_add_f32 v[60:61], v[240:241], v[60:61]
	v_pk_add_f32 v[54:55], v[238:239], v[54:55]
	v_pk_add_f32 v[44:45], v[92:93], v[44:45]
	v_pk_add_f32 v[42:43], v[90:91], v[42:43]
	v_pk_add_f32 v[32:33], v[68:69], v[32:33]
	v_pk_add_f32 v[30:31], v[62:63], v[30:31]
	v_pk_add_f32 v[22:23], v[48:49], v[22:23]
	v_pk_add_f32 v[18:19], v[46:47], v[18:19]
	v_pk_add_f32 v[34:35], v[8:9], v[6:7]
	v_pk_add_f32 v[36:37], v[2:3], v[0:1]
	s_waitcnt lgkmcnt(0)
	v_lshl_add_u64 v[38:39], s[6:7], 0, v[4:5]
	v_add_u32_e32 v6, 16, v4
	v_add_u32_e32 v8, 32, v4
	v_add_u32_e32 v12, 0x1000, v4
	v_add_u32_e32 v16, 0x1020, v4
	v_lshl_add_u64 v[122:123], v[38:39], 0, s[18:19]
	global_load_dwordx4 v[0:3], v4, s[0:1]
	v_pk_mul_f32 v[26:27], v[110:111], s[24:25] op_sel_hi:[1,0]
	v_pk_mul_f32 v[96:97], v[118:119], s[24:25] op_sel_hi:[1,0]
	v_pk_mul_f32 v[98:99], v[54:55], s[24:25] op_sel_hi:[1,0]
	v_pk_mul_f32 v[100:101], v[60:61], s[24:25] op_sel_hi:[1,0]
	v_add_u32_e32 v10, 48, v4
	v_pk_mul_f32 v[102:103], v[42:43], s[24:25] op_sel_hi:[1,0]
	v_pk_mul_f32 v[104:105], v[44:45], s[24:25] op_sel_hi:[1,0]
	v_pk_mul_f32 v[106:107], v[30:31], s[24:25] op_sel_hi:[1,0]
	v_pk_mul_f32 v[108:109], v[32:33], s[24:25] op_sel_hi:[1,0]
	v_add_u32_e32 v14, 0x1010, v4
	v_pk_mul_f32 v[110:111], v[18:19], s[24:25] op_sel_hi:[1,0]
	v_add_u32_e32 v18, 0x1030, v4
	v_pk_mul_f32 v[118:119], v[36:37], s[24:25] op_sel_hi:[1,0]
	v_pk_mul_f32 v[120:121], v[34:35], s[24:25] op_sel_hi:[1,0]
	global_load_dwordx4 v[30:33], v6, s[0:1]
	global_load_dwordx4 v[34:37], v8, s[0:1]
	global_load_dwordx4 v[38:41], v10, s[0:1]
	global_load_dwordx4 v[42:45], v12, s[0:1]
	global_load_dwordx4 v[46:49], v14, s[0:1]
	global_load_dwordx4 v[50:53], v16, s[0:1]
	global_load_dwordx4 v[54:57], v18, s[0:1]
	global_load_dwordx4 v[58:61], v[122:123], off
	v_mov_b32_e32 v7, v5
	v_pk_mul_f32 v[28:29], v[116:117], s[24:25] op_sel_hi:[1,0]
	v_mov_b32_e32 v9, v5
	v_mov_b32_e32 v11, v5
	v_mov_b32_e32 v13, v5
	v_mov_b32_e32 v15, v5
	v_mov_b32_e32 v17, v5
	v_pk_mul_f32 v[116:117], v[20:21], s[24:25] op_sel_hi:[1,0]
	v_mov_b32_e32 v19, v5
	v_lshl_add_u64 v[20:21], s[6:7], 0, v[6:7]
	v_pk_mul_f32 v[94:95], v[112:113], s[24:25] op_sel_hi:[1,0]
	v_pk_mul_f32 v[112:113], v[22:23], s[24:25] op_sel_hi:[1,0]
	v_pk_mul_f32 v[114:115], v[24:25], s[24:25] op_sel_hi:[1,0]
	v_lshl_add_u64 v[22:23], s[6:7], 0, v[8:9]
	v_lshl_add_u64 v[24:25], s[6:7], 0, v[10:11]
	v_lshl_add_u64 v[62:63], s[6:7], 0, v[12:13]
	v_lshl_add_u64 v[64:65], s[6:7], 0, v[14:15]
	v_lshl_add_u64 v[66:67], s[6:7], 0, v[16:17]
	v_lshl_add_u64 v[68:69], s[6:7], 0, v[18:19]
	v_lshl_add_u64 v[124:125], v[20:21], 0, s[18:19]
	v_lshl_add_u64 v[132:133], v[22:23], 0, s[18:19]
	v_lshl_add_u64 v[134:135], v[24:25], 0, s[18:19]
	v_lshl_add_u64 v[136:137], v[62:63], 0, s[18:19]
	v_lshl_add_u64 v[24:25], v[64:65], 0, s[18:19]
	v_lshl_add_u64 v[22:23], v[66:67], 0, s[18:19]
	v_lshl_add_u64 v[20:21], v[68:69], 0, s[18:19]
	global_load_dwordx4 v[62:65], v[124:125], off
	global_load_dwordx4 v[66:69], v[132:133], off
	global_load_dwordx4 v[70:73], v[134:135], off
	global_load_dwordx4 v[74:77], v[136:137], off
	global_load_dwordx4 v[78:81], v[24:25], off
	global_load_dwordx4 v[82:85], v[22:23], off
	global_load_dwordx4 v[86:89], v[20:21], off
	global_load_dwordx4 v[90:93], v4, s[4:5]
	s_add_i32 s42, s42, s56
	s_add_u32 s10, s10, s12
	s_addc_u32 s11, s11, s13
	s_add_u32 s14, s14, s16
	s_addc_u32 s15, s15, s17
	s_add_u32 s18, s18, s20
	s_addc_u32 s19, s19, s21
	s_cmpk_lt_i32 s42, 0x2000
	s_waitcnt vmcnt(8)
	v_pk_fma_f32 v[2:3], v[2:3], v[28:29], v[60:61]
	v_pk_fma_f32 v[0:1], v[0:1], v[26:27], v[58:59]
	v_mul_f32_e32 v7, v3, v3
	v_mul_f32_e32 v4, v1, v1
	v_fmac_f32_e32 v4, v0, v0
	v_fmac_f32_e32 v7, v2, v2
	v_add_f32_e32 v4, v4, v7
	s_waitcnt vmcnt(7)
	v_pk_fma_f32 v[26:27], v[32:33], v[96:97], v[64:65]
	v_pk_fma_f32 v[28:29], v[30:31], v[94:95], v[62:63]
	s_waitcnt vmcnt(6)
	v_pk_fma_f32 v[30:31], v[36:37], v[100:101], v[68:69]
	v_pk_fma_f32 v[32:33], v[34:35], v[98:99], v[66:67]
	v_mul_f32_e32 v9, v29, v29
	v_mul_f32_e32 v11, v27, v27
	s_waitcnt vmcnt(5)
	v_pk_fma_f32 v[34:35], v[40:41], v[104:105], v[72:73]
	v_pk_fma_f32 v[36:37], v[38:39], v[102:103], v[70:71]
	v_mul_f32_e32 v13, v33, v33
	v_mul_f32_e32 v15, v31, v31
	v_fmac_f32_e32 v9, v28, v28
	v_fmac_f32_e32 v11, v26, v26
	s_waitcnt vmcnt(4)
	v_pk_fma_f32 v[38:39], v[44:45], v[108:109], v[76:77]
	v_pk_fma_f32 v[40:41], v[42:43], v[106:107], v[74:75]
	v_mul_f32_e32 v17, v37, v37
	v_mul_f32_e32 v19, v35, v35
	v_fmac_f32_e32 v13, v32, v32
	v_fmac_f32_e32 v15, v30, v30
	v_add_f32_e32 v7, v9, v11
	s_waitcnt vmcnt(3)
	v_pk_fma_f32 v[42:43], v[48:49], v[112:113], v[80:81]
	v_pk_fma_f32 v[44:45], v[46:47], v[110:111], v[78:79]
	s_waitcnt vmcnt(2)
	v_pk_fma_f32 v[46:47], v[52:53], v[116:117], v[84:85]
	s_waitcnt vmcnt(1)
	global_load_dwordx4 v[62:65], v5, s[14:15]
	global_load_dwordx4 v[70:73], v5, s[14:15] offset:16
	global_load_dwordx4 v[138:141], v6, s[4:5]
	global_load_dwordx4 v[142:145], v8, s[4:5]
	global_load_dwordx4 v[146:149], v10, s[4:5]
	global_load_dwordx4 v[150:153], v12, s[4:5]
	global_load_dwordx4 v[244:247], v14, s[4:5]
	global_load_dwordx4 v[248:251], v16, s[4:5]
	global_load_dwordx4 v[252:255], v18, s[4:5]
	v_pk_fma_f32 v[52:53], v[54:55], v[118:119], v[86:87]
	v_mul_f32_e32 v54, v41, v41
	v_mul_f32_e32 v55, v39, v39
	v_fmac_f32_e32 v17, v36, v36
	v_fmac_f32_e32 v19, v34, v34
	v_add_f32_e32 v9, v13, v15
	v_add_f32_e32 v4, v4, v7
	v_pk_fma_f32 v[48:49], v[50:51], v[114:115], v[82:83]
	v_pk_fma_f32 v[50:51], v[56:57], v[120:121], v[88:89]
	v_mul_f32_e32 v56, v45, v45
	v_mul_f32_e32 v57, v43, v43
	v_fmac_f32_e32 v54, v40, v40
	v_fmac_f32_e32 v55, v38, v38
	v_add_f32_e32 v11, v17, v19
	v_add_f32_e32 v4, v4, v9
	v_mul_f32_e32 v58, v49, v49
	v_mul_f32_e32 v59, v47, v47
	v_fmac_f32_e32 v56, v44, v44
	v_fmac_f32_e32 v57, v42, v42
	v_add_f32_e32 v13, v54, v55
	v_add_f32_e32 v4, v4, v11
	v_mul_f32_e32 v60, v53, v53
	v_mul_f32_e32 v61, v51, v51
	v_fmac_f32_e32 v58, v48, v48
	v_fmac_f32_e32 v59, v46, v46
	v_add_f32_e32 v15, v56, v57
	v_add_f32_e32 v4, v4, v13
	v_fmac_f32_e32 v60, v52, v52
	v_fmac_f32_e32 v61, v50, v50
	v_add_f32_e32 v17, v58, v59
	v_add_f32_e32 v4, v4, v15
	v_add_f32_e32 v19, v60, v61
	v_add_f32_e32 v4, v4, v17
	v_add_f32_e32 v4, v4, v19
	ds_swizzle_b32 v7, v4 offset:swizzle(SWAP,1)
	s_waitcnt lgkmcnt(0)
	v_add_f32_e32 v4, v4, v7
	ds_swizzle_b32 v7, v4 offset:swizzle(SWAP,2)
	s_waitcnt lgkmcnt(0)
	v_add_f32_e32 v4, v4, v7
	ds_swizzle_b32 v7, v4 offset:swizzle(SWAP,4)
	s_waitcnt lgkmcnt(0)
	v_add_f32_e32 v4, v4, v7
	ds_swizzle_b32 v7, v4 offset:swizzle(SWAP,8)
	s_waitcnt lgkmcnt(0)
	v_add_f32_e32 v4, v4, v7
	ds_swizzle_b32 v7, v4 offset:swizzle(SWAP,16)
	s_waitcnt lgkmcnt(0)
	v_add_f32_e32 v4, v4, v7
	v_mov_b32_e32 v7, v4
	s_nop 1
	v_permlane32_swap_b32_e32 v4, v7
	v_add_f32_e32 v4, v4, v7
	v_fmamk_f32 v4, v4, 0x3a000000, v129
	v_mul_f32_e32 v7, 0x4f800000, v4
	v_cmp_gt_f32_e32 vcc, s28, v4
	s_nop 1
	v_cndmask_b32_e32 v4, v4, v7, vcc
	v_sqrt_f32_e32 v7, v4
	s_nop 0
	v_add_u32_e32 v9, -1, v7
	v_add_u32_e32 v11, 1, v7
	v_fma_f32 v13, -v9, v7, v4
	v_fma_f32 v15, -v11, v7, v4
	v_cmp_ge_f32_e64 s[0:1], 0, v13
	s_nop 1
	v_cndmask_b32_e64 v7, v7, v9, s[0:1]
	v_cmp_lt_f32_e64 s[0:1], 0, v15
	s_nop 1
	v_cndmask_b32_e64 v7, v7, v11, s[0:1]
	v_mul_f32_e32 v9, 0x37800000, v7
	v_cndmask_b32_e32 v7, v7, v9, vcc
	v_cmp_class_f32_e32 vcc, v4, v130
	s_nop 1
	v_cndmask_b32_e32 v4, v7, v4, vcc
	v_div_scale_f32 v7, s[0:1], v4, v4, 1.0
	v_rcp_f32_e32 v11, v7
	v_div_scale_f32 v9, vcc, 1.0, v4, 1.0
	v_fma_f32 v13, -v7, v11, 1.0
	v_fmac_f32_e32 v11, v13, v11
	v_mul_f32_e32 v13, v9, v11
	v_fma_f32 v15, -v7, v13, v9
	v_fmac_f32_e32 v13, v15, v11
	v_fma_f32 v7, -v7, v13, v9
	v_div_fmas_f32 v7, v7, v11, v13
	v_div_fixup_f32 v4, v7, v4, 1.0
	v_pk_mul_f32 v[0:1], v[4:5], v[0:1] op_sel_hi:[0,1]
	v_pk_mul_f32 v[2:3], v[4:5], v[2:3] op_sel_hi:[0,1]
	s_waitcnt vmcnt(0)
	v_pk_mul_f32 v[2:3], v[2:3], v[92:93]
	v_pk_mul_f32 v[0:1], v[0:1], v[90:91]
	global_store_dwordx4 v[122:123], v[0:3], off
	v_pk_mul_f32 v[6:7], v[4:5], v[26:27] op_sel_hi:[0,1]
	v_pk_mul_f32 v[26:27], v[4:5], v[28:29] op_sel_hi:[0,1]
	v_pk_mul_f32 v[0:1], v[26:27], v[138:139]
	v_pk_mul_f32 v[2:3], v[6:7], v[140:141]
	global_store_dwordx4 v[124:125], v[0:3], off
	v_pk_mul_f32 v[6:7], v[4:5], v[30:31] op_sel_hi:[0,1]
	v_pk_mul_f32 v[8:9], v[4:5], v[32:33] op_sel_hi:[0,1]
	v_pk_mul_f32 v[0:1], v[8:9], v[142:143]
	v_pk_mul_f32 v[2:3], v[6:7], v[144:145]
	global_store_dwordx4 v[132:133], v[0:3], off
	v_pk_mul_f32 v[6:7], v[4:5], v[34:35] op_sel_hi:[0,1]
	v_pk_mul_f32 v[8:9], v[4:5], v[36:37] op_sel_hi:[0,1]
	v_pk_mul_f32 v[0:1], v[8:9], v[146:147]
	v_pk_mul_f32 v[2:3], v[6:7], v[148:149]
	global_store_dwordx4 v[134:135], v[0:3], off
	v_pk_mul_f32 v[6:7], v[4:5], v[38:39] op_sel_hi:[0,1]
	v_pk_mul_f32 v[8:9], v[4:5], v[40:41] op_sel_hi:[0,1]
	v_pk_mul_f32 v[0:1], v[8:9], v[150:151]
	v_pk_mul_f32 v[2:3], v[6:7], v[152:153]
	global_store_dwordx4 v[136:137], v[0:3], off
	v_pk_mul_f32 v[6:7], v[4:5], v[42:43] op_sel_hi:[0,1]
	v_pk_mul_f32 v[8:9], v[4:5], v[44:45] op_sel_hi:[0,1]
	v_pk_mul_f32 v[0:1], v[8:9], v[244:245]
	v_pk_mul_f32 v[2:3], v[6:7], v[246:247]
	global_store_dwordx4 v[24:25], v[0:3], off
	v_pk_mul_f32 v[6:7], v[4:5], v[46:47] op_sel_hi:[0,1]
	v_pk_mul_f32 v[8:9], v[4:5], v[48:49] op_sel_hi:[0,1]
	v_pk_mul_f32 v[0:1], v[8:9], v[248:249]
	v_pk_mul_f32 v[2:3], v[6:7], v[250:251]
	global_store_dwordx4 v[22:23], v[0:3], off
	v_pk_mul_f32 v[6:7], v[4:5], v[50:51] op_sel_hi:[0,1]
	v_pk_mul_f32 v[8:9], v[4:5], v[52:53] op_sel_hi:[0,1]
	v_pk_mul_f32 v[0:1], v[8:9], v[252:253]
	v_pk_mul_f32 v[2:3], v[6:7], v[254:255]
	global_store_dwordx4 v[20:21], v[0:3], off
	s_cbranch_scc1 .LBB0_1206
